# baseline (speedup 1.0000x reference)
.LBB3_1:
	s_waitcnt vmcnt(4)
	s_lshl_b32 s18, s23, 14
	s_barrier
	v_or_b32_e32 v144, s18, v115
	v_add_u32_e32 v154, v144, v116
	v_add_u32_e32 v155, v144, v117
	v_add_u32_e32 v156, v144, v118
	v_add_u32_e32 v157, v144, v119
	ds_read_b128 v[50:53], v154
	ds_read_b128 v[120:123], v154 offset:4096
	ds_read_b128 v[124:127], v155
	ds_read_b128 v[128:131], v155 offset:4096
	ds_read_b128 v[132:135], v156
	ds_read_b128 v[136:139], v156 offset:4096
	ds_read_b128 v[140:143], v157
	ds_read_b128 v[150:153], v157 offset:4096
	s_waitcnt lgkmcnt(4)
	s_setprio 1
	v_mfma_f32_32x32x16_f16 v[66:81], v[50:53], v[94:97], v[34:49]
	v_mfma_f32_32x32x16_f16 v[50:65], v[120:123], v[94:97], v[34:49]
	v_mfma_f32_32x32x16_f16 v[66:81], v[124:127], v[90:93], v[66:81]
	v_mfma_f32_32x32x16_f16 v[50:65], v[128:131], v[90:93], v[50:65]
	s_waitcnt lgkmcnt(0)
	v_mfma_f32_32x32x16_f16 v[66:81], v[132:135], v[86:89], v[66:81]
	v_mfma_f32_32x32x16_f16 v[50:65], v[136:139], v[86:89], v[50:65]
	v_mfma_f32_32x32x16_f16 v[66:81], v[140:143], v[82:85], v[66:81]
	v_mfma_f32_32x32x16_f16 v[50:65], v[150:153], v[82:85], v[50:65]
	s_setprio 0
	s_cmp_gt_u32 s9, 13
	s_mov_b64 s[6:7], -1
	s_cbranch_scc0 .LBB3_3
	s_sleep 1
	s_mov_b64 s[6:7], 0
